# scanner refills its load ring in bursts of 4 consecutive 1 KB pieces (20-deep ring) instead of one piece at a time
# speedup vs baseline: 1.0010x; 1.0010x over previous
.Lsc_row:
	v_subrev_u32_e32 v8, s47, v3
	v_lshlrev_b32_e32 v8, 2, v8
	s_add_i32 s41, s47, 3
	v_min_u32_e32 v4, s41, v3
	v_lshlrev_b32_e32 v4, 4, v4
	s_lshl_b64 s[48:49], -1, s47
	s_add_i32 s41, s47, 3
	s_lshl_b64 s[50:51], 2, s41
	s_sub_u32 s50, s50, 1
	s_subb_u32 s51, s51, 0
	s_and_b32 s41, s35, 1
	s_lshl_b32 s40, s41, 11
	s_add_u32 s40, s40, s44
	v_mov_b32_e32 v9, s40
	s_lshl_b32 s40, s41, 9
	s_add_u32 s40, s40, s45
	v_mov_b32_e32 v10, s40
	s_lshl_b32 s40, s41, 2
	s_add_u32 s40, s40, s46
	v_mov_b32_e32 v11, s40
	s_cmp_lt_i32 s35, s36
	s_cbranch_scc0 .Lsc_nonext
	s_add_i32 s52, s37, s33
	s_and_b32 s53, s52, 1
	s_lshl_b32 s53, s53, 2
	s_mul_i32 s39, s52, 0x9c40
	s_lshl_b32 s40, s53, 4
	s_sub_u32 s39, s39, s40
	v_max_u32_e32 v5, s53, v3
	v_lshlrev_b32_e32 v5, 4, v5
	v_mov_b32_e32 v6, v2
	s_add_i32 s40, s53, 3
	v_min_u32_e32 v7, s40, v3
	v_lshlrev_b32_e32 v7, 4, v7
	s_branch .Lsc_gotnext

.Lsc_s0:
	s_waitcnt vmcnt(18)
	v_or3_b32 v12, v104, v105, v106
	v_bitop3_b32 v12, v12, s9, v107 bitop3:0xc8
	v_cmp_ne_u32_e32 vcc, 0, v12
	s_cbranch_vccz .Lsc_s1
	s_nop 0
	v_mbcnt_lo_u32_b32 v13, vcc_lo, 0
	v_mbcnt_hi_u32_b32 v13, vcc_hi, v13
	v_add_u32_e32 v13, s42, v13
	v_cmp_gt_i32_e64 s[0:1], s7, v13
	s_and_b64 s[4:5], vcc, s[0:1]
	s_and_saveexec_b64 s[0:1], s[4:5]
	v_lshl_add_u32 v14, v13, 4, v9
	v_lshl_add_u32 v15, v13, 2, v10
	v_add_u32_e32 v13, 0x100, v8
	ds_write_b128 v14, v[104:107]
	ds_write_b32 v15, v13
	s_mov_b64 exec, -1
	s_bcnt1_i32_b64 s40, vcc
	s_add_i32 s42, s42, s40
.Lsc_s1:
	s_waitcnt vmcnt(17)
	v_or3_b32 v12, v108, v109, v110
	v_bitop3_b32 v12, v12, s9, v111 bitop3:0xc8
	v_cmp_ne_u32_e32 vcc, 0, v12
	s_cbranch_vccz .Lsc_s2
	s_nop 0
	v_mbcnt_lo_u32_b32 v13, vcc_lo, 0
	v_mbcnt_hi_u32_b32 v13, vcc_hi, v13
	v_add_u32_e32 v13, s42, v13
	v_cmp_gt_i32_e64 s[0:1], s7, v13
	s_and_b64 s[4:5], vcc, s[0:1]
	s_and_saveexec_b64 s[0:1], s[4:5]
	v_lshl_add_u32 v14, v13, 4, v9
	v_lshl_add_u32 v15, v13, 2, v10
	v_add_u32_e32 v13, 0x200, v8
	ds_write_b128 v14, v[108:111]
	ds_write_b32 v15, v13
	s_mov_b64 exec, -1
	s_bcnt1_i32_b64 s40, vcc
	s_add_i32 s42, s42, s40
.Lsc_s2:
	s_waitcnt vmcnt(16)
	v_or3_b32 v12, v112, v113, v114
	v_bitop3_b32 v12, v12, s9, v115 bitop3:0xc8
	v_cmp_ne_u32_e32 vcc, 0, v12
	s_cbranch_vccz .Lsc_s3
	s_nop 0
	v_mbcnt_lo_u32_b32 v13, vcc_lo, 0
	v_mbcnt_hi_u32_b32 v13, vcc_hi, v13
	v_add_u32_e32 v13, s42, v13
	v_cmp_gt_i32_e64 s[0:1], s7, v13
	s_and_b64 s[4:5], vcc, s[0:1]
	s_and_saveexec_b64 s[0:1], s[4:5]
	v_lshl_add_u32 v14, v13, 4, v9
	v_lshl_add_u32 v15, v13, 2, v10
	v_add_u32_e32 v13, 0x300, v8
	ds_write_b128 v14, v[112:115]
	ds_write_b32 v15, v13
	s_mov_b64 exec, -1
	s_bcnt1_i32_b64 s40, vcc
	s_add_i32 s42, s42, s40
.Lsc_s3:
	s_add_u32 s40, s38, 0x5000
	buffer_load_dwordx4 v[100:103], v2, s[28:31], s40 offen nt
	s_add_u32 s40, s38, 0x5400
	buffer_load_dwordx4 v[104:107], v2, s[28:31], s40 offen nt
	s_add_u32 s40, s38, 0x5800
	buffer_load_dwordx4 v[108:111], v2, s[28:31], s40 offen nt
	s_add_u32 s40, s38, 0x5c00
	buffer_load_dwordx4 v[112:115], v2, s[28:31], s40 offen nt
	s_waitcnt vmcnt(19)
	v_or3_b32 v12, v116, v117, v118
	v_bitop3_b32 v12, v12, s9, v119 bitop3:0xc8
	v_cmp_ne_u32_e32 vcc, 0, v12
	s_cbranch_vccz .Lsc_s4
	s_nop 0
	v_mbcnt_lo_u32_b32 v13, vcc_lo, 0
	v_mbcnt_hi_u32_b32 v13, vcc_hi, v13
	v_add_u32_e32 v13, s42, v13
	v_cmp_gt_i32_e64 s[0:1], s7, v13
	s_and_b64 s[4:5], vcc, s[0:1]
	s_and_saveexec_b64 s[0:1], s[4:5]
	v_lshl_add_u32 v14, v13, 4, v9
	v_lshl_add_u32 v15, v13, 2, v10
	v_add_u32_e32 v13, 0x400, v8
	ds_write_b128 v14, v[116:119]
	ds_write_b32 v15, v13
	s_mov_b64 exec, -1
	s_bcnt1_i32_b64 s40, vcc
	s_add_i32 s42, s42, s40
.Lsc_s4:
	s_waitcnt vmcnt(18)
	v_or3_b32 v12, v120, v121, v122
	v_bitop3_b32 v12, v12, s9, v123 bitop3:0xc8
	v_cmp_ne_u32_e32 vcc, 0, v12
	s_cbranch_vccz .Lsc_s5
	s_nop 0
	v_mbcnt_lo_u32_b32 v13, vcc_lo, 0
	v_mbcnt_hi_u32_b32 v13, vcc_hi, v13
	v_add_u32_e32 v13, s42, v13
	v_cmp_gt_i32_e64 s[0:1], s7, v13
	s_and_b64 s[4:5], vcc, s[0:1]
	s_and_saveexec_b64 s[0:1], s[4:5]
	v_lshl_add_u32 v14, v13, 4, v9
	v_lshl_add_u32 v15, v13, 2, v10
	v_add_u32_e32 v13, 0x500, v8
	ds_write_b128 v14, v[120:123]
	ds_write_b32 v15, v13
	s_mov_b64 exec, -1
	s_bcnt1_i32_b64 s40, vcc
	s_add_i32 s42, s42, s40
.Lsc_s5:
	s_waitcnt vmcnt(17)
	v_or3_b32 v12, v124, v125, v126
	v_bitop3_b32 v12, v12, s9, v127 bitop3:0xc8
	v_cmp_ne_u32_e32 vcc, 0, v12
	s_cbranch_vccz .Lsc_s6
	s_nop 0
	v_mbcnt_lo_u32_b32 v13, vcc_lo, 0
	v_mbcnt_hi_u32_b32 v13, vcc_hi, v13
	v_add_u32_e32 v13, s42, v13
	v_cmp_gt_i32_e64 s[0:1], s7, v13
	s_and_b64 s[4:5], vcc, s[0:1]
	s_and_saveexec_b64 s[0:1], s[4:5]
	v_lshl_add_u32 v14, v13, 4, v9
	v_lshl_add_u32 v15, v13, 2, v10
	v_add_u32_e32 v13, 0x600, v8
	ds_write_b128 v14, v[124:127]
	ds_write_b32 v15, v13
	s_mov_b64 exec, -1
	s_bcnt1_i32_b64 s40, vcc
	s_add_i32 s42, s42, s40
.Lsc_s6:
	s_waitcnt vmcnt(16)
	v_or3_b32 v12, v128, v129, v130
	v_bitop3_b32 v12, v12, s9, v131 bitop3:0xc8
	v_cmp_ne_u32_e32 vcc, 0, v12
	s_cbranch_vccz .Lsc_s7
	s_nop 0
	v_mbcnt_lo_u32_b32 v13, vcc_lo, 0
	v_mbcnt_hi_u32_b32 v13, vcc_hi, v13
	v_add_u32_e32 v13, s42, v13
	v_cmp_gt_i32_e64 s[0:1], s7, v13
	s_and_b64 s[4:5], vcc, s[0:1]
	s_and_saveexec_b64 s[0:1], s[4:5]
	v_lshl_add_u32 v14, v13, 4, v9
	v_lshl_add_u32 v15, v13, 2, v10
	v_add_u32_e32 v13, 0x700, v8
	ds_write_b128 v14, v[128:131]
	ds_write_b32 v15, v13
	s_mov_b64 exec, -1
	s_bcnt1_i32_b64 s40, vcc
	s_add_i32 s42, s42, s40
.Lsc_s7:
	s_add_u32 s40, s38, 0x6000
	buffer_load_dwordx4 v[116:119], v2, s[28:31], s40 offen nt
	s_add_u32 s40, s38, 0x6400
	buffer_load_dwordx4 v[120:123], v2, s[28:31], s40 offen nt
	s_add_u32 s40, s38, 0x6800
	buffer_load_dwordx4 v[124:127], v2, s[28:31], s40 offen nt
	s_add_u32 s40, s38, 0x6c00
	buffer_load_dwordx4 v[128:131], v2, s[28:31], s40 offen nt
	s_waitcnt vmcnt(19)
	v_or3_b32 v12, v132, v133, v134
	v_bitop3_b32 v12, v12, s9, v135 bitop3:0xc8
	v_cmp_ne_u32_e32 vcc, 0, v12
	s_cbranch_vccz .Lsc_s8
	s_nop 0
	v_mbcnt_lo_u32_b32 v13, vcc_lo, 0
	v_mbcnt_hi_u32_b32 v13, vcc_hi, v13
	v_add_u32_e32 v13, s42, v13
	v_cmp_gt_i32_e64 s[0:1], s7, v13
	s_and_b64 s[4:5], vcc, s[0:1]
	s_and_saveexec_b64 s[0:1], s[4:5]
	v_lshl_add_u32 v14, v13, 4, v9
	v_lshl_add_u32 v15, v13, 2, v10
	v_add_u32_e32 v13, 0x800, v8
	ds_write_b128 v14, v[132:135]
	ds_write_b32 v15, v13
	s_mov_b64 exec, -1
	s_bcnt1_i32_b64 s40, vcc
	s_add_i32 s42, s42, s40
.Lsc_s8:
	s_waitcnt vmcnt(18)
	v_or3_b32 v12, v136, v137, v138
	v_bitop3_b32 v12, v12, s9, v139 bitop3:0xc8
	v_cmp_ne_u32_e32 vcc, 0, v12
	s_cbranch_vccz .Lsc_s9
	s_nop 0
	v_mbcnt_lo_u32_b32 v13, vcc_lo, 0
	v_mbcnt_hi_u32_b32 v13, vcc_hi, v13
	v_add_u32_e32 v13, s42, v13
	v_cmp_gt_i32_e64 s[0:1], s7, v13
	s_and_b64 s[4:5], vcc, s[0:1]
	s_and_saveexec_b64 s[0:1], s[4:5]
	v_lshl_add_u32 v14, v13, 4, v9
	v_lshl_add_u32 v15, v13, 2, v10
	v_add_u32_e32 v13, 0x900, v8
	ds_write_b128 v14, v[136:139]
	ds_write_b32 v15, v13
	s_mov_b64 exec, -1
	s_bcnt1_i32_b64 s40, vcc
	s_add_i32 s42, s42, s40
.Lsc_s9:
	s_waitcnt vmcnt(17)
	v_or3_b32 v12, v140, v141, v142
	v_bitop3_b32 v12, v12, s9, v143 bitop3:0xc8
	v_cmp_ne_u32_e32 vcc, 0, v12
	s_cbranch_vccz .Lsc_s10
	s_nop 0
	v_mbcnt_lo_u32_b32 v13, vcc_lo, 0
	v_mbcnt_hi_u32_b32 v13, vcc_hi, v13
	v_add_u32_e32 v13, s42, v13
	v_cmp_gt_i32_e64 s[0:1], s7, v13
	s_and_b64 s[4:5], vcc, s[0:1]
	s_and_saveexec_b64 s[0:1], s[4:5]
	v_lshl_add_u32 v14, v13, 4, v9
	v_lshl_add_u32 v15, v13, 2, v10
	v_add_u32_e32 v13, 0xa00, v8
	ds_write_b128 v14, v[140:143]
	ds_write_b32 v15, v13
	s_mov_b64 exec, -1
	s_bcnt1_i32_b64 s40, vcc
	s_add_i32 s42, s42, s40
.Lsc_s10:
	s_waitcnt vmcnt(16)
	v_or3_b32 v12, v144, v145, v146
	v_bitop3_b32 v12, v12, s9, v147 bitop3:0xc8
	v_cmp_ne_u32_e32 vcc, 0, v12
	s_cbranch_vccz .Lsc_s11
	s_nop 0
	v_mbcnt_lo_u32_b32 v13, vcc_lo, 0
	v_mbcnt_hi_u32_b32 v13, vcc_hi, v13
	v_add_u32_e32 v13, s42, v13
	v_cmp_gt_i32_e64 s[0:1], s7, v13
	s_and_b64 s[4:5], vcc, s[0:1]
	s_and_saveexec_b64 s[0:1], s[4:5]
	v_lshl_add_u32 v14, v13, 4, v9
	v_lshl_add_u32 v15, v13, 2, v10
	v_add_u32_e32 v13, 0xb00, v8
	ds_write_b128 v14, v[144:147]
	ds_write_b32 v15, v13
	s_mov_b64 exec, -1
	s_bcnt1_i32_b64 s40, vcc
	s_add_i32 s42, s42, s40
.Lsc_s11:
	s_add_u32 s40, s38, 0x7000
	buffer_load_dwordx4 v[132:135], v2, s[28:31], s40 offen nt
	s_add_u32 s40, s38, 0x7400
	buffer_load_dwordx4 v[136:139], v2, s[28:31], s40 offen nt
	s_add_u32 s40, s38, 0x7800
	buffer_load_dwordx4 v[140:143], v2, s[28:31], s40 offen nt
	s_add_u32 s40, s38, 0x7c00
	buffer_load_dwordx4 v[144:147], v2, s[28:31], s40 offen nt
	s_waitcnt vmcnt(19)
	v_or3_b32 v12, v148, v149, v150
	v_bitop3_b32 v12, v12, s9, v151 bitop3:0xc8
	v_cmp_ne_u32_e32 vcc, 0, v12
	s_cbranch_vccz .Lsc_s12
	s_nop 0
	v_mbcnt_lo_u32_b32 v13, vcc_lo, 0
	v_mbcnt_hi_u32_b32 v13, vcc_hi, v13
	v_add_u32_e32 v13, s42, v13
	v_cmp_gt_i32_e64 s[0:1], s7, v13
	s_and_b64 s[4:5], vcc, s[0:1]
	s_and_saveexec_b64 s[0:1], s[4:5]
	v_lshl_add_u32 v14, v13, 4, v9
	v_lshl_add_u32 v15, v13, 2, v10
	v_add_u32_e32 v13, 0xc00, v8
	ds_write_b128 v14, v[148:151]
	ds_write_b32 v15, v13
	s_mov_b64 exec, -1
	s_bcnt1_i32_b64 s40, vcc
	s_add_i32 s42, s42, s40
.Lsc_s12:
	s_waitcnt vmcnt(18)
	v_or3_b32 v12, v152, v153, v154
	v_bitop3_b32 v12, v12, s9, v155 bitop3:0xc8
	v_cmp_ne_u32_e32 vcc, 0, v12
	s_cbranch_vccz .Lsc_s13
	s_nop 0
	v_mbcnt_lo_u32_b32 v13, vcc_lo, 0
	v_mbcnt_hi_u32_b32 v13, vcc_hi, v13
	v_add_u32_e32 v13, s42, v13
	v_cmp_gt_i32_e64 s[0:1], s7, v13
	s_and_b64 s[4:5], vcc, s[0:1]
	s_and_saveexec_b64 s[0:1], s[4:5]
	v_lshl_add_u32 v14, v13, 4, v9
	v_lshl_add_u32 v15, v13, 2, v10
	v_add_u32_e32 v13, 0xd00, v8
	ds_write_b128 v14, v[152:155]
	ds_write_b32 v15, v13
	s_mov_b64 exec, -1
	s_bcnt1_i32_b64 s40, vcc
	s_add_i32 s42, s42, s40
.Lsc_s13:
	s_waitcnt vmcnt(17)
	v_or3_b32 v12, v156, v157, v158
	v_bitop3_b32 v12, v12, s9, v159 bitop3:0xc8
	v_cmp_ne_u32_e32 vcc, 0, v12
	s_cbranch_vccz .Lsc_s14
	s_nop 0
	v_mbcnt_lo_u32_b32 v13, vcc_lo, 0
	v_mbcnt_hi_u32_b32 v13, vcc_hi, v13
	v_add_u32_e32 v13, s42, v13
	v_cmp_gt_i32_e64 s[0:1], s7, v13
	s_and_b64 s[4:5], vcc, s[0:1]
	s_and_saveexec_b64 s[0:1], s[4:5]
	v_lshl_add_u32 v14, v13, 4, v9
	v_lshl_add_u32 v15, v13, 2, v10
	v_add_u32_e32 v13, 0xe00, v8
	ds_write_b128 v14, v[156:159]
	ds_write_b32 v15, v13
	s_mov_b64 exec, -1
	s_bcnt1_i32_b64 s40, vcc
	s_add_i32 s42, s42, s40
.Lsc_s14:
	s_waitcnt vmcnt(16)
	v_or3_b32 v12, v160, v161, v162
	v_bitop3_b32 v12, v12, s9, v163 bitop3:0xc8
	v_cmp_ne_u32_e32 vcc, 0, v12
	s_cbranch_vccz .Lsc_s15
	s_nop 0
	v_mbcnt_lo_u32_b32 v13, vcc_lo, 0
	v_mbcnt_hi_u32_b32 v13, vcc_hi, v13
	v_add_u32_e32 v13, s42, v13
	v_cmp_gt_i32_e64 s[0:1], s7, v13
	s_and_b64 s[4:5], vcc, s[0:1]
	s_and_saveexec_b64 s[0:1], s[4:5]
	v_lshl_add_u32 v14, v13, 4, v9
	v_lshl_add_u32 v15, v13, 2, v10
	v_add_u32_e32 v13, 0xf00, v8
	ds_write_b128 v14, v[160:163]
	ds_write_b32 v15, v13
	s_mov_b64 exec, -1
	s_bcnt1_i32_b64 s40, vcc
	s_add_i32 s42, s42, s40
.Lsc_s15:
	s_add_u32 s40, s38, 0x8000
	buffer_load_dwordx4 v[148:151], v2, s[28:31], s40 offen nt
	s_add_u32 s40, s38, 0x8400
	buffer_load_dwordx4 v[152:155], v2, s[28:31], s40 offen nt
	s_add_u32 s40, s38, 0x8800
	buffer_load_dwordx4 v[156:159], v2, s[28:31], s40 offen nt
	s_add_u32 s40, s38, 0x8c00
	buffer_load_dwordx4 v[160:163], v2, s[28:31], s40 offen nt
	s_waitcnt vmcnt(19)
	v_or3_b32 v12, v164, v165, v166
	v_bitop3_b32 v12, v12, s9, v167 bitop3:0xc8
	v_cmp_ne_u32_e32 vcc, 0, v12
	s_cbranch_vccz .Lsc_s16
	s_nop 0
	v_mbcnt_lo_u32_b32 v13, vcc_lo, 0
	v_mbcnt_hi_u32_b32 v13, vcc_hi, v13
	v_add_u32_e32 v13, s42, v13
	v_cmp_gt_i32_e64 s[0:1], s7, v13
	s_and_b64 s[4:5], vcc, s[0:1]
	s_and_saveexec_b64 s[0:1], s[4:5]
	v_lshl_add_u32 v14, v13, 4, v9
	v_lshl_add_u32 v15, v13, 2, v10
	v_add_u32_e32 v13, 0x1000, v8
	ds_write_b128 v14, v[164:167]
	ds_write_b32 v15, v13
	s_mov_b64 exec, -1
	s_bcnt1_i32_b64 s40, vcc
	s_add_i32 s42, s42, s40
.Lsc_s16:
	s_waitcnt vmcnt(18)
	v_or3_b32 v12, v168, v169, v170
	v_bitop3_b32 v12, v12, s9, v171 bitop3:0xc8
	v_cmp_ne_u32_e32 vcc, 0, v12
	s_cbranch_vccz .Lsc_s17
	s_nop 0
	v_mbcnt_lo_u32_b32 v13, vcc_lo, 0
	v_mbcnt_hi_u32_b32 v13, vcc_hi, v13
	v_add_u32_e32 v13, s42, v13
	v_cmp_gt_i32_e64 s[0:1], s7, v13
	s_and_b64 s[4:5], vcc, s[0:1]
	s_and_saveexec_b64 s[0:1], s[4:5]
	v_lshl_add_u32 v14, v13, 4, v9
	v_lshl_add_u32 v15, v13, 2, v10
	v_add_u32_e32 v13, 0x1100, v8
	ds_write_b128 v14, v[168:171]
	ds_write_b32 v15, v13
	s_mov_b64 exec, -1
	s_bcnt1_i32_b64 s40, vcc
	s_add_i32 s42, s42, s40
.Lsc_s17:
	s_waitcnt vmcnt(17)
	v_or3_b32 v12, v172, v173, v174
	v_bitop3_b32 v12, v12, s9, v175 bitop3:0xc8
	v_cmp_ne_u32_e32 vcc, 0, v12
	s_cbranch_vccz .Lsc_s18
	s_nop 0
	v_mbcnt_lo_u32_b32 v13, vcc_lo, 0
	v_mbcnt_hi_u32_b32 v13, vcc_hi, v13
	v_add_u32_e32 v13, s42, v13
	v_cmp_gt_i32_e64 s[0:1], s7, v13
	s_and_b64 s[4:5], vcc, s[0:1]
	s_and_saveexec_b64 s[0:1], s[4:5]
	v_lshl_add_u32 v14, v13, 4, v9
	v_lshl_add_u32 v15, v13, 2, v10
	v_add_u32_e32 v13, 0x1200, v8
	ds_write_b128 v14, v[172:175]
	ds_write_b32 v15, v13
	s_mov_b64 exec, -1
	s_bcnt1_i32_b64 s40, vcc
	s_add_i32 s42, s42, s40
.Lsc_s18:
	s_waitcnt vmcnt(16)
	v_or3_b32 v12, v176, v177, v178
	v_bitop3_b32 v12, v12, s9, v179 bitop3:0xc8
	v_cmp_ne_u32_e32 vcc, 0, v12
	s_cbranch_vccz .Lsc_s19
	s_nop 0
	v_mbcnt_lo_u32_b32 v13, vcc_lo, 0
	v_mbcnt_hi_u32_b32 v13, vcc_hi, v13
	v_add_u32_e32 v13, s42, v13
	v_cmp_gt_i32_e64 s[0:1], s7, v13
	s_and_b64 s[4:5], vcc, s[0:1]
	s_and_saveexec_b64 s[0:1], s[4:5]
	v_lshl_add_u32 v14, v13, 4, v9
	v_lshl_add_u32 v15, v13, 2, v10
	v_add_u32_e32 v13, 0x1300, v8
	ds_write_b128 v14, v[176:179]
	ds_write_b32 v15, v13
	s_mov_b64 exec, -1
	s_bcnt1_i32_b64 s40, vcc
	s_add_i32 s42, s42, s40
.Lsc_s19:
	s_add_u32 s40, s38, 0x9000
	buffer_load_dwordx4 v[164:167], v2, s[28:31], s40 offen nt
	s_add_u32 s40, s38, 0x9400
	buffer_load_dwordx4 v[168:171], v2, s[28:31], s40 offen nt
	s_add_u32 s40, s38, 0x9800
	buffer_load_dwordx4 v[172:175], v2, s[28:31], s40 offen nt
	s_add_u32 s40, s38, 0x9c00
	buffer_load_dwordx4 v[176:179], v4, s[28:31], s40 offen nt
	s_waitcnt vmcnt(19)
	v_or3_b32 v12, v100, v101, v102
	v_bitop3_b32 v12, v12, s9, v103 bitop3:0xc8
	v_cmp_ne_u32_e32 vcc, 0, v12
	s_cbranch_vccz .Lsc_s20
	s_nop 0
	v_mbcnt_lo_u32_b32 v13, vcc_lo, 0
	v_mbcnt_hi_u32_b32 v13, vcc_hi, v13
	v_add_u32_e32 v13, s42, v13
	v_cmp_gt_i32_e64 s[0:1], s7, v13
	s_and_b64 s[4:5], vcc, s[0:1]
	s_and_saveexec_b64 s[0:1], s[4:5]
	v_lshl_add_u32 v14, v13, 4, v9
	v_lshl_add_u32 v15, v13, 2, v10
	v_add_u32_e32 v13, 0x1400, v8
	ds_write_b128 v14, v[100:103]
	ds_write_b32 v15, v13
	s_mov_b64 exec, -1
	s_bcnt1_i32_b64 s40, vcc
	s_add_i32 s42, s42, s40
.Lsc_s20:
	s_waitcnt vmcnt(18)
	v_or3_b32 v12, v104, v105, v106
	v_bitop3_b32 v12, v12, s9, v107 bitop3:0xc8
	v_cmp_ne_u32_e32 vcc, 0, v12
	s_cbranch_vccz .Lsc_s21
	s_nop 0
	v_mbcnt_lo_u32_b32 v13, vcc_lo, 0
	v_mbcnt_hi_u32_b32 v13, vcc_hi, v13
	v_add_u32_e32 v13, s42, v13
	v_cmp_gt_i32_e64 s[0:1], s7, v13
	s_and_b64 s[4:5], vcc, s[0:1]
	s_and_saveexec_b64 s[0:1], s[4:5]
	v_lshl_add_u32 v14, v13, 4, v9
	v_lshl_add_u32 v15, v13, 2, v10
	v_add_u32_e32 v13, 0x1500, v8
	ds_write_b128 v14, v[104:107]
	ds_write_b32 v15, v13
	s_mov_b64 exec, -1
	s_bcnt1_i32_b64 s40, vcc
	s_add_i32 s42, s42, s40
.Lsc_s21:
	s_waitcnt vmcnt(17)
	v_or3_b32 v12, v108, v109, v110
	v_bitop3_b32 v12, v12, s9, v111 bitop3:0xc8
	v_cmp_ne_u32_e32 vcc, 0, v12
	s_cbranch_vccz .Lsc_s22
	s_nop 0
	v_mbcnt_lo_u32_b32 v13, vcc_lo, 0
	v_mbcnt_hi_u32_b32 v13, vcc_hi, v13
	v_add_u32_e32 v13, s42, v13
	v_cmp_gt_i32_e64 s[0:1], s7, v13
	s_and_b64 s[4:5], vcc, s[0:1]
	s_and_saveexec_b64 s[0:1], s[4:5]
	v_lshl_add_u32 v14, v13, 4, v9
	v_lshl_add_u32 v15, v13, 2, v10
	v_add_u32_e32 v13, 0x1600, v8
	ds_write_b128 v14, v[108:111]
	ds_write_b32 v15, v13
	s_mov_b64 exec, -1
	s_bcnt1_i32_b64 s40, vcc
	s_add_i32 s42, s42, s40
.Lsc_s22:
	s_waitcnt vmcnt(16)
	v_or3_b32 v12, v112, v113, v114
	v_bitop3_b32 v12, v12, s9, v115 bitop3:0xc8
	v_cmp_ne_u32_e32 vcc, 0, v12
	s_cbranch_vccz .Lsc_s23
	s_nop 0
	v_mbcnt_lo_u32_b32 v13, vcc_lo, 0
	v_mbcnt_hi_u32_b32 v13, vcc_hi, v13
	v_add_u32_e32 v13, s42, v13
	v_cmp_gt_i32_e64 s[0:1], s7, v13
	s_and_b64 s[4:5], vcc, s[0:1]
	s_and_saveexec_b64 s[0:1], s[4:5]
	v_lshl_add_u32 v14, v13, 4, v9
	v_lshl_add_u32 v15, v13, 2, v10
	v_add_u32_e32 v13, 0x1700, v8
	ds_write_b128 v14, v[112:115]
	ds_write_b32 v15, v13
	s_mov_b64 exec, -1
	s_bcnt1_i32_b64 s40, vcc
	s_add_i32 s42, s42, s40
.Lsc_s23:
	s_mov_b32 s40, s39
	buffer_load_dwordx4 v[100:103], v5, s[28:31], s40 offen nt
	s_add_u32 s40, s39, 0x400
	buffer_load_dwordx4 v[104:107], v6, s[28:31], s40 offen nt
	s_add_u32 s40, s39, 0x800
	buffer_load_dwordx4 v[108:111], v6, s[28:31], s40 offen nt
	s_add_u32 s40, s39, 0xc00
	buffer_load_dwordx4 v[112:115], v6, s[28:31], s40 offen nt
	s_waitcnt vmcnt(19)
	v_or3_b32 v12, v116, v117, v118
	v_bitop3_b32 v12, v12, s9, v119 bitop3:0xc8
	v_cmp_ne_u32_e32 vcc, 0, v12
	s_cbranch_vccz .Lsc_s24
	s_nop 0
	v_mbcnt_lo_u32_b32 v13, vcc_lo, 0
	v_mbcnt_hi_u32_b32 v13, vcc_hi, v13
	v_add_u32_e32 v13, s42, v13
	v_cmp_gt_i32_e64 s[0:1], s7, v13
	s_and_b64 s[4:5], vcc, s[0:1]
	s_and_saveexec_b64 s[0:1], s[4:5]
	v_lshl_add_u32 v14, v13, 4, v9
	v_lshl_add_u32 v15, v13, 2, v10
	v_add_u32_e32 v13, 0x1800, v8
	ds_write_b128 v14, v[116:119]
	ds_write_b32 v15, v13
	s_mov_b64 exec, -1
	s_bcnt1_i32_b64 s40, vcc
	s_add_i32 s42, s42, s40
.Lsc_s24:
	s_waitcnt vmcnt(18)
	v_or3_b32 v12, v120, v121, v122
	v_bitop3_b32 v12, v12, s9, v123 bitop3:0xc8
	v_cmp_ne_u32_e32 vcc, 0, v12
	s_cbranch_vccz .Lsc_s25
	s_nop 0
	v_mbcnt_lo_u32_b32 v13, vcc_lo, 0
	v_mbcnt_hi_u32_b32 v13, vcc_hi, v13
	v_add_u32_e32 v13, s42, v13
	v_cmp_gt_i32_e64 s[0:1], s7, v13
	s_and_b64 s[4:5], vcc, s[0:1]
	s_and_saveexec_b64 s[0:1], s[4:5]
	v_lshl_add_u32 v14, v13, 4, v9
	v_lshl_add_u32 v15, v13, 2, v10
	v_add_u32_e32 v13, 0x1900, v8
	ds_write_b128 v14, v[120:123]
	ds_write_b32 v15, v13
	s_mov_b64 exec, -1
	s_bcnt1_i32_b64 s40, vcc
	s_add_i32 s42, s42, s40
.Lsc_s25:
	s_waitcnt vmcnt(17)
	v_or3_b32 v12, v124, v125, v126
	v_bitop3_b32 v12, v12, s9, v127 bitop3:0xc8
	v_cmp_ne_u32_e32 vcc, 0, v12
	s_cbranch_vccz .Lsc_s26
	s_nop 0
	v_mbcnt_lo_u32_b32 v13, vcc_lo, 0
	v_mbcnt_hi_u32_b32 v13, vcc_hi, v13
	v_add_u32_e32 v13, s42, v13
	v_cmp_gt_i32_e64 s[0:1], s7, v13
	s_and_b64 s[4:5], vcc, s[0:1]
	s_and_saveexec_b64 s[0:1], s[4:5]
	v_lshl_add_u32 v14, v13, 4, v9
	v_lshl_add_u32 v15, v13, 2, v10
	v_add_u32_e32 v13, 0x1a00, v8
	ds_write_b128 v14, v[124:127]
	ds_write_b32 v15, v13
	s_mov_b64 exec, -1
	s_bcnt1_i32_b64 s40, vcc
	s_add_i32 s42, s42, s40
.Lsc_s26:
	s_waitcnt vmcnt(16)
	v_or3_b32 v12, v128, v129, v130
	v_bitop3_b32 v12, v12, s9, v131 bitop3:0xc8
	v_cmp_ne_u32_e32 vcc, 0, v12
	s_cbranch_vccz .Lsc_s27
	s_nop 0
	v_mbcnt_lo_u32_b32 v13, vcc_lo, 0
	v_mbcnt_hi_u32_b32 v13, vcc_hi, v13
	v_add_u32_e32 v13, s42, v13
	v_cmp_gt_i32_e64 s[0:1], s7, v13
	s_and_b64 s[4:5], vcc, s[0:1]
	s_and_saveexec_b64 s[0:1], s[4:5]
	v_lshl_add_u32 v14, v13, 4, v9
	v_lshl_add_u32 v15, v13, 2, v10
	v_add_u32_e32 v13, 0x1b00, v8
	ds_write_b128 v14, v[128:131]
	ds_write_b32 v15, v13
	s_mov_b64 exec, -1
	s_bcnt1_i32_b64 s40, vcc
	s_add_i32 s42, s42, s40
.Lsc_s27:
	s_add_u32 s40, s39, 0x1000
	buffer_load_dwordx4 v[116:119], v6, s[28:31], s40 offen nt
	s_add_u32 s40, s39, 0x1400
	buffer_load_dwordx4 v[120:123], v6, s[28:31], s40 offen nt
	s_add_u32 s40, s39, 0x1800
	buffer_load_dwordx4 v[124:127], v6, s[28:31], s40 offen nt
	s_add_u32 s40, s39, 0x1c00
	buffer_load_dwordx4 v[128:131], v6, s[28:31], s40 offen nt
	s_waitcnt vmcnt(19)
	v_or3_b32 v12, v132, v133, v134
	v_bitop3_b32 v12, v12, s9, v135 bitop3:0xc8
	v_cmp_ne_u32_e32 vcc, 0, v12
	s_cbranch_vccz .Lsc_s28
	s_nop 0
	v_mbcnt_lo_u32_b32 v13, vcc_lo, 0
	v_mbcnt_hi_u32_b32 v13, vcc_hi, v13
	v_add_u32_e32 v13, s42, v13
	v_cmp_gt_i32_e64 s[0:1], s7, v13
	s_and_b64 s[4:5], vcc, s[0:1]
	s_and_saveexec_b64 s[0:1], s[4:5]
	v_lshl_add_u32 v14, v13, 4, v9
	v_lshl_add_u32 v15, v13, 2, v10
	v_add_u32_e32 v13, 0x1c00, v8
	ds_write_b128 v14, v[132:135]
	ds_write_b32 v15, v13
	s_mov_b64 exec, -1
	s_bcnt1_i32_b64 s40, vcc
	s_add_i32 s42, s42, s40
.Lsc_s28:
	s_waitcnt vmcnt(18)
	v_or3_b32 v12, v136, v137, v138
	v_bitop3_b32 v12, v12, s9, v139 bitop3:0xc8
	v_cmp_ne_u32_e32 vcc, 0, v12
	s_cbranch_vccz .Lsc_s29
	s_nop 0
	v_mbcnt_lo_u32_b32 v13, vcc_lo, 0
	v_mbcnt_hi_u32_b32 v13, vcc_hi, v13
	v_add_u32_e32 v13, s42, v13
	v_cmp_gt_i32_e64 s[0:1], s7, v13
	s_and_b64 s[4:5], vcc, s[0:1]
	s_and_saveexec_b64 s[0:1], s[4:5]
	v_lshl_add_u32 v14, v13, 4, v9
	v_lshl_add_u32 v15, v13, 2, v10
	v_add_u32_e32 v13, 0x1d00, v8
	ds_write_b128 v14, v[136:139]
	ds_write_b32 v15, v13
	s_mov_b64 exec, -1
	s_bcnt1_i32_b64 s40, vcc
	s_add_i32 s42, s42, s40
.Lsc_s29:
	s_waitcnt vmcnt(17)
	v_or3_b32 v12, v140, v141, v142
	v_bitop3_b32 v12, v12, s9, v143 bitop3:0xc8
	v_cmp_ne_u32_e32 vcc, 0, v12
	s_cbranch_vccz .Lsc_s30
	s_nop 0
	v_mbcnt_lo_u32_b32 v13, vcc_lo, 0
	v_mbcnt_hi_u32_b32 v13, vcc_hi, v13
	v_add_u32_e32 v13, s42, v13
	v_cmp_gt_i32_e64 s[0:1], s7, v13
	s_and_b64 s[4:5], vcc, s[0:1]
	s_and_saveexec_b64 s[0:1], s[4:5]
	v_lshl_add_u32 v14, v13, 4, v9
	v_lshl_add_u32 v15, v13, 2, v10
	v_add_u32_e32 v13, 0x1e00, v8
	ds_write_b128 v14, v[140:143]
	ds_write_b32 v15, v13
	s_mov_b64 exec, -1
	s_bcnt1_i32_b64 s40, vcc
	s_add_i32 s42, s42, s40
.Lsc_s30:
	s_waitcnt vmcnt(16)
	v_or3_b32 v12, v144, v145, v146
	v_bitop3_b32 v12, v12, s9, v147 bitop3:0xc8
	v_cmp_ne_u32_e32 vcc, 0, v12
	s_cbranch_vccz .Lsc_s31
	s_nop 0
	v_mbcnt_lo_u32_b32 v13, vcc_lo, 0
	v_mbcnt_hi_u32_b32 v13, vcc_hi, v13
	v_add_u32_e32 v13, s42, v13
	v_cmp_gt_i32_e64 s[0:1], s7, v13
	s_and_b64 s[4:5], vcc, s[0:1]
	s_and_saveexec_b64 s[0:1], s[4:5]
	v_lshl_add_u32 v14, v13, 4, v9
	v_lshl_add_u32 v15, v13, 2, v10
	v_add_u32_e32 v13, 0x1f00, v8
	ds_write_b128 v14, v[144:147]
	ds_write_b32 v15, v13
	s_mov_b64 exec, -1
	s_bcnt1_i32_b64 s40, vcc
	s_add_i32 s42, s42, s40
.Lsc_s31:
	s_add_u32 s40, s39, 0x2000
	buffer_load_dwordx4 v[132:135], v6, s[28:31], s40 offen nt
	s_add_u32 s40, s39, 0x2400
	buffer_load_dwordx4 v[136:139], v6, s[28:31], s40 offen nt
	s_add_u32 s40, s39, 0x2800
	buffer_load_dwordx4 v[140:143], v6, s[28:31], s40 offen nt
	s_add_u32 s40, s39, 0x2c00
	buffer_load_dwordx4 v[144:147], v6, s[28:31], s40 offen nt
	s_waitcnt vmcnt(19)
	v_or3_b32 v12, v148, v149, v150
	v_bitop3_b32 v12, v12, s9, v151 bitop3:0xc8
	v_cmp_ne_u32_e32 vcc, 0, v12
	s_cbranch_vccz .Lsc_s32
	s_nop 0
	v_mbcnt_lo_u32_b32 v13, vcc_lo, 0
	v_mbcnt_hi_u32_b32 v13, vcc_hi, v13
	v_add_u32_e32 v13, s42, v13
	v_cmp_gt_i32_e64 s[0:1], s7, v13
	s_and_b64 s[4:5], vcc, s[0:1]
	s_and_saveexec_b64 s[0:1], s[4:5]
	v_lshl_add_u32 v14, v13, 4, v9
	v_lshl_add_u32 v15, v13, 2, v10
	v_add_u32_e32 v13, 0x2000, v8
	ds_write_b128 v14, v[148:151]
	ds_write_b32 v15, v13
	s_mov_b64 exec, -1
	s_bcnt1_i32_b64 s40, vcc
	s_add_i32 s42, s42, s40
.Lsc_s32:
	s_waitcnt vmcnt(18)
	v_or3_b32 v12, v152, v153, v154
	v_bitop3_b32 v12, v12, s9, v155 bitop3:0xc8
	v_cmp_ne_u32_e32 vcc, 0, v12
	s_cbranch_vccz .Lsc_s33
	s_nop 0
	v_mbcnt_lo_u32_b32 v13, vcc_lo, 0
	v_mbcnt_hi_u32_b32 v13, vcc_hi, v13
	v_add_u32_e32 v13, s42, v13
	v_cmp_gt_i32_e64 s[0:1], s7, v13
	s_and_b64 s[4:5], vcc, s[0:1]
	s_and_saveexec_b64 s[0:1], s[4:5]
	v_lshl_add_u32 v14, v13, 4, v9
	v_lshl_add_u32 v15, v13, 2, v10
	v_add_u32_e32 v13, 0x2100, v8
	ds_write_b128 v14, v[152:155]
	ds_write_b32 v15, v13
	s_mov_b64 exec, -1
	s_bcnt1_i32_b64 s40, vcc
	s_add_i32 s42, s42, s40
.Lsc_s33:
	s_waitcnt vmcnt(17)
	v_or3_b32 v12, v156, v157, v158
	v_bitop3_b32 v12, v12, s9, v159 bitop3:0xc8
	v_cmp_ne_u32_e32 vcc, 0, v12
	s_cbranch_vccz .Lsc_s34
	s_nop 0
	v_mbcnt_lo_u32_b32 v13, vcc_lo, 0
	v_mbcnt_hi_u32_b32 v13, vcc_hi, v13
	v_add_u32_e32 v13, s42, v13
	v_cmp_gt_i32_e64 s[0:1], s7, v13
	s_and_b64 s[4:5], vcc, s[0:1]
	s_and_saveexec_b64 s[0:1], s[4:5]
	v_lshl_add_u32 v14, v13, 4, v9
	v_lshl_add_u32 v15, v13, 2, v10
	v_add_u32_e32 v13, 0x2200, v8
	ds_write_b128 v14, v[156:159]
	ds_write_b32 v15, v13
	s_mov_b64 exec, -1
	s_bcnt1_i32_b64 s40, vcc
	s_add_i32 s42, s42, s40
.Lsc_s34:
	s_waitcnt vmcnt(16)
	v_or3_b32 v12, v160, v161, v162
	v_bitop3_b32 v12, v12, s9, v163 bitop3:0xc8
	v_cmp_ne_u32_e32 vcc, 0, v12
	s_cbranch_vccz .Lsc_s35
	s_nop 0
	v_mbcnt_lo_u32_b32 v13, vcc_lo, 0
	v_mbcnt_hi_u32_b32 v13, vcc_hi, v13
	v_add_u32_e32 v13, s42, v13
	v_cmp_gt_i32_e64 s[0:1], s7, v13
	s_and_b64 s[4:5], vcc, s[0:1]
	s_and_saveexec_b64 s[0:1], s[4:5]
	v_lshl_add_u32 v14, v13, 4, v9
	v_lshl_add_u32 v15, v13, 2, v10
	v_add_u32_e32 v13, 0x2300, v8
	ds_write_b128 v14, v[160:163]
	ds_write_b32 v15, v13
	s_mov_b64 exec, -1
	s_bcnt1_i32_b64 s40, vcc
	s_add_i32 s42, s42, s40
.Lsc_s35:
	s_add_u32 s40, s39, 0x3000
	buffer_load_dwordx4 v[148:151], v6, s[28:31], s40 offen nt
	s_add_u32 s40, s39, 0x3400
	buffer_load_dwordx4 v[152:155], v6, s[28:31], s40 offen nt
	s_add_u32 s40, s39, 0x3800
	buffer_load_dwordx4 v[156:159], v6, s[28:31], s40 offen nt
	s_add_u32 s40, s39, 0x3c00
	buffer_load_dwordx4 v[160:163], v6, s[28:31], s40 offen nt
	s_waitcnt vmcnt(19)
	v_or3_b32 v12, v164, v165, v166
	v_bitop3_b32 v12, v12, s9, v167 bitop3:0xc8
	v_cmp_ne_u32_e32 vcc, 0, v12
	s_cbranch_vccz .Lsc_s36
	s_nop 0
	v_mbcnt_lo_u32_b32 v13, vcc_lo, 0
	v_mbcnt_hi_u32_b32 v13, vcc_hi, v13
	v_add_u32_e32 v13, s42, v13
	v_cmp_gt_i32_e64 s[0:1], s7, v13
	s_and_b64 s[4:5], vcc, s[0:1]
	s_and_saveexec_b64 s[0:1], s[4:5]
	v_lshl_add_u32 v14, v13, 4, v9
	v_lshl_add_u32 v15, v13, 2, v10
	v_add_u32_e32 v13, 0x2400, v8
	ds_write_b128 v14, v[164:167]
	ds_write_b32 v15, v13
	s_mov_b64 exec, -1
	s_bcnt1_i32_b64 s40, vcc
	s_add_i32 s42, s42, s40
.Lsc_s36:
	s_waitcnt vmcnt(18)
	v_or3_b32 v12, v168, v169, v170
	v_bitop3_b32 v12, v12, s9, v171 bitop3:0xc8
	v_cmp_ne_u32_e32 vcc, 0, v12
	s_cbranch_vccz .Lsc_s37
	s_nop 0
	v_mbcnt_lo_u32_b32 v13, vcc_lo, 0
	v_mbcnt_hi_u32_b32 v13, vcc_hi, v13
	v_add_u32_e32 v13, s42, v13
	v_cmp_gt_i32_e64 s[0:1], s7, v13
	s_and_b64 s[4:5], vcc, s[0:1]
	s_and_saveexec_b64 s[0:1], s[4:5]
	v_lshl_add_u32 v14, v13, 4, v9
	v_lshl_add_u32 v15, v13, 2, v10
	v_add_u32_e32 v13, 0x2500, v8
	ds_write_b128 v14, v[168:171]
	ds_write_b32 v15, v13
	s_mov_b64 exec, -1
	s_bcnt1_i32_b64 s40, vcc
	s_add_i32 s42, s42, s40
.Lsc_s37:
	s_waitcnt vmcnt(17)
	v_or3_b32 v12, v172, v173, v174
	v_bitop3_b32 v12, v12, s9, v175 bitop3:0xc8
	v_cmp_ne_u32_e32 vcc, 0, v12
	s_cbranch_vccz .Lsc_s38
	s_nop 0
	v_mbcnt_lo_u32_b32 v13, vcc_lo, 0
	v_mbcnt_hi_u32_b32 v13, vcc_hi, v13
	v_add_u32_e32 v13, s42, v13
	v_cmp_gt_i32_e64 s[0:1], s7, v13
	s_and_b64 s[4:5], vcc, s[0:1]
	s_and_saveexec_b64 s[0:1], s[4:5]
	v_lshl_add_u32 v14, v13, 4, v9
	v_lshl_add_u32 v15, v13, 2, v10
	v_add_u32_e32 v13, 0x2600, v8
	ds_write_b128 v14, v[172:175]
	ds_write_b32 v15, v13
	s_mov_b64 exec, -1
	s_bcnt1_i32_b64 s40, vcc
	s_add_i32 s42, s42, s40
.Lsc_s38:
	s_waitcnt vmcnt(16)
	v_or3_b32 v12, v176, v177, v178
	v_bitop3_b32 v12, v12, s9, v179 bitop3:0xc8
	v_cmp_ne_u32_e32 vcc, 0, v12
	s_and_b64 vcc, vcc, s[50:51]
	s_cbranch_vccz .Lsc_s39
	s_nop 0
	v_mbcnt_lo_u32_b32 v13, vcc_lo, 0
	v_mbcnt_hi_u32_b32 v13, vcc_hi, v13
	v_add_u32_e32 v13, s42, v13
	v_cmp_gt_i32_e64 s[0:1], s7, v13
	s_and_b64 s[4:5], vcc, s[0:1]
	s_and_saveexec_b64 s[0:1], s[4:5]
	v_lshl_add_u32 v14, v13, 4, v9
	v_lshl_add_u32 v15, v13, 2, v10
	v_add_u32_e32 v13, 0x2700, v8
	ds_write_b128 v14, v[176:179]
	ds_write_b32 v15, v13
	s_mov_b64 exec, -1
	s_bcnt1_i32_b64 s40, vcc
	s_add_i32 s42, s42, s40
.Lsc_s39:
	s_add_u32 s40, s39, 0x4000
	buffer_load_dwordx4 v[164:167], v6, s[28:31], s40 offen nt
	s_add_u32 s40, s39, 0x4400
	buffer_load_dwordx4 v[168:171], v6, s[28:31], s40 offen nt
	s_add_u32 s40, s39, 0x4800
	buffer_load_dwordx4 v[172:175], v6, s[28:31], s40 offen nt
	s_add_u32 s40, s39, 0x4c00
	buffer_load_dwordx4 v[176:179], v6, s[28:31], s40 offen nt
	s_waitcnt lgkmcnt(0)
	s_add_i32 s42, s42, 1
	v_mov_b32_e32 v12, s42
	ds_write_b32 v11, v12
	s_cmp_eq_u32 s35, s36
	s_cbranch_scc1 .LBB1_384
	s_add_i32 s35, s35, 1
	s_mov_b32 s37, s52
	s_mov_b32 s38, s39
	s_mov_b32 s47, s53
	s_branch .Lsc_row
